# norm1 / norm2 gain-and-shift staging: the two-iteration load loop unrolled, 12 loads in flight
# baseline (speedup 1.0000x reference)
; __device__ __forceinline__ void phase_norm1(const Ptrs& p, LAS unsigned char* lds) {
;     ...
;         __syncthreads();
;         for (int i = tid; i < 2048; i += 512) { gs[i] = p.norm_mix_g[i] * (1.0f + mod[D + i]); sh[i] = mod[i]; }
;         __syncthreads();
.LBB0_110:
	v_ashrrev_i32_e32 v7, 31, v3
	v_mov_b32_e32 v6, v3
	v_ashrrev_i32_e32 v9, 31, v2
	v_mov_b32_e32 v8, v2
	v_lshlrev_b64 v[8:9], 2, v[8:9]
	v_lshlrev_b64 v[6:7], 2, v[6:7]
	v_lshl_add_u64 v[24:25], s[60:61], 0, v[8:9]
	v_lshl_add_u64 v[64:65], s[60:61], 0, v[6:7]
	v_lshl_add_u64 v[8:9], s[34:35], 0, v[8:9]
	global_load_dword v24, v[24:25], off
	s_nop 0
	global_load_dword v25, v[64:65], off
	v_add_co_u32_e32 v64, vcc, s54, v8
	v_lshl_add_u64 v[6:7], s[34:35], 0, v[6:7]
	s_nop 0
	v_addc_co_u32_e32 v65, vcc, 0, v9, vcc
	v_add_co_u32_e32 v66, vcc, s54, v6
	v_add_u32_e32 v3, 0x400, v3
	s_nop 0
	v_addc_co_u32_e32 v67, vcc, 0, v7, vcc
	global_load_dword v5, v[8:9], off
	s_nop 0
	global_load_dword v8, v[64:65], off
	global_load_dword v9, v[66:67], off
	global_load_dword v23, v[6:7], off
	v_add_u32_e32 v6, s28, v4
	s_addk_i32 s28, 0x1000
	v_add_u32_e32 v7, 0x22200, v6
	v_add_u32_e32 v64, 0x20200, v6
	v_add_u32_e32 v65, 0x20a00, v6
	v_add_u32_e32 v66, 0x22a00, v6
	v_cmp_eq_u32_e32 vcc, s28, v55
	v_add_u32_e32 v2, 0x400, v2
	s_or_b64 s[40:41], vcc, s[40:41]
	v_ashrrev_i32_e32 v123, 31, v3
	v_mov_b32_e32 v122, v3
	v_ashrrev_i32_e32 v125, 31, v2
	v_mov_b32_e32 v124, v2
	v_lshlrev_b64 v[124:125], 2, v[124:125]
	v_lshlrev_b64 v[122:123], 2, v[122:123]
	v_lshl_add_u64 v[128:129], s[60:61], 0, v[124:125]
	v_lshl_add_u64 v[130:131], s[60:61], 0, v[122:123]
	v_lshl_add_u64 v[124:125], s[34:35], 0, v[124:125]
	global_load_dword v128, v[128:129], off
	s_nop 0
	global_load_dword v129, v[130:131], off
	v_add_co_u32_e32 v130, vcc, s54, v124
	v_lshl_add_u64 v[122:123], s[34:35], 0, v[122:123]
	s_nop 0
	v_addc_co_u32_e32 v131, vcc, 0, v125, vcc
	v_add_co_u32_e32 v132, vcc, s54, v122
	v_add_u32_e32 v3, 0x400, v3
	s_nop 0
	v_addc_co_u32_e32 v133, vcc, 0, v123, vcc
	global_load_dword v120, v[124:125], off
	s_nop 0
	global_load_dword v124, v[130:131], off
	global_load_dword v125, v[132:133], off
	global_load_dword v126, v[122:123], off
	v_add_u32_e32 v122, s28, v4
	s_addk_i32 s28, 0x1000
	v_add_u32_e32 v123, 0x22200, v122
	v_add_u32_e32 v130, 0x20200, v122
	v_add_u32_e32 v131, 0x20a00, v122
	v_add_u32_e32 v132, 0x22a00, v122
	v_cmp_eq_u32_e32 vcc, s28, v55
	v_add_u32_e32 v2, 0x400, v2
	s_or_b64 s[40:41], vcc, s[40:41]
	s_waitcnt vmcnt(9)
	ds_write_b32 v7, v5
	s_waitcnt vmcnt(7)
	v_pk_add_f32 v[6:7], v[8:9], 1.0 op_sel_hi:[1,0]
	s_nop 0
	v_pk_mul_f32 v[6:7], v[24:25], v[6:7]
	s_waitcnt vmcnt(6)
	ds_write_b32 v66, v23
	ds_write_b32 v64, v6
	ds_write_b32 v65, v7
	s_waitcnt vmcnt(3)
	ds_write_b32 v123, v120
	s_waitcnt vmcnt(1)
	v_pk_add_f32 v[122:123], v[124:125], 1.0 op_sel_hi:[1,0]
	s_nop 0
	v_pk_mul_f32 v[122:123], v[128:129], v[122:123]
	s_waitcnt vmcnt(0)
	ds_write_b32 v132, v126
	ds_write_b32 v130, v122
	ds_write_b32 v131, v123

; __device__ __forceinline__ void phase_norm2_route(const Ptrs& p, LAS unsigned char* lds) {
;     ...
;         __syncthreads();
;         for (int i = tid; i < 2048; i += 512) { gs[i] = p.norm_ffn_g[i] * (1.0f + mod[4 * D + i]); sh[i] = mod[3 * D + i]; }
;         __syncthreads();
.LBB0_916:
	v_ashrrev_i32_e32 v7, 31, v3
	v_mov_b32_e32 v6, v3
	v_ashrrev_i32_e32 v9, 31, v2
	v_mov_b32_e32 v8, v2
	v_lshlrev_b64 v[8:9], 2, v[8:9]
	v_lshlrev_b64 v[6:7], 2, v[6:7]
	v_lshl_add_u64 v[10:11], s[42:43], 0, v[8:9]
	v_lshl_add_u64 v[12:13], s[42:43], 0, v[6:7]
	v_lshl_add_u64 v[8:9], s[58:59], 0, v[8:9]
	global_load_dword v10, v[10:11], off
	s_nop 0
	global_load_dword v11, v[12:13], off
	v_add_co_u32_e32 v12, vcc, s66, v8
	v_lshl_add_u64 v[6:7], s[58:59], 0, v[6:7]
	s_nop 0
	v_addc_co_u32_e32 v13, vcc, 0, v9, vcc
	v_add_co_u32_e32 v14, vcc, s66, v6
	v_add_u32_e32 v3, 0x400, v3
	s_nop 0
	v_addc_co_u32_e32 v15, vcc, 0, v7, vcc
	v_add_co_u32_e32 v8, vcc, s67, v8
	v_add_u32_e32 v2, 0x400, v2
	s_nop 0
	v_addc_co_u32_e32 v9, vcc, 0, v9, vcc
	global_load_dword v12, v[12:13], off
	s_nop 0
	global_load_dword v13, v[14:15], off
	global_load_dword v5, v[8:9], off
	v_add_co_u32_e32 v6, vcc, 0x6000, v6
	s_nop 1
	v_addc_co_u32_e32 v7, vcc, 0, v7, vcc
	global_load_dword v8, v[6:7], off
	v_add_u32_e32 v6, s28, v4
	s_addk_i32 s28, 0x1000
	v_cmp_eq_u32_e32 vcc, s28, v175
	v_add_u32_e32 v9, 0x20800, v6
	v_add_u32_e32 v14, 0x21000, v6
	v_add_u32_e32 v15, 0x22800, v6
	v_add_u32_e32 v16, 0x23000, v6
	s_or_b64 s[62:63], vcc, s[62:63]
	v_ashrrev_i32_e32 v219, 31, v3
	v_mov_b32_e32 v218, v3
	v_ashrrev_i32_e32 v221, 31, v2
	v_mov_b32_e32 v220, v2
	v_lshlrev_b64 v[220:221], 2, v[220:221]
	v_lshlrev_b64 v[218:219], 2, v[218:219]
	v_lshl_add_u64 v[222:223], s[42:43], 0, v[220:221]
	v_lshl_add_u64 v[224:225], s[42:43], 0, v[218:219]
	v_lshl_add_u64 v[220:221], s[58:59], 0, v[220:221]
	global_load_dword v222, v[222:223], off
	s_nop 0
	global_load_dword v223, v[224:225], off
	v_add_co_u32_e32 v224, vcc, s66, v220
	v_lshl_add_u64 v[218:219], s[58:59], 0, v[218:219]
	s_nop 0
	v_addc_co_u32_e32 v225, vcc, 0, v221, vcc
	v_add_co_u32_e32 v226, vcc, s66, v218
	v_add_u32_e32 v3, 0x400, v3
	s_nop 0
	v_addc_co_u32_e32 v227, vcc, 0, v219, vcc
	v_add_co_u32_e32 v220, vcc, s67, v220
	v_add_u32_e32 v2, 0x400, v2
	s_nop 0
	v_addc_co_u32_e32 v221, vcc, 0, v221, vcc
	global_load_dword v224, v[224:225], off
	s_nop 0
	global_load_dword v225, v[226:227], off
	global_load_dword v216, v[220:221], off
	v_add_co_u32_e32 v218, vcc, 0x6000, v218
	s_nop 1
	v_addc_co_u32_e32 v219, vcc, 0, v219, vcc
	global_load_dword v220, v[218:219], off
	v_add_u32_e32 v218, s28, v4
	s_addk_i32 s28, 0x1000
	v_cmp_eq_u32_e32 vcc, s28, v175
	v_add_u32_e32 v221, 0x20800, v218
	v_add_u32_e32 v226, 0x21000, v218
	v_add_u32_e32 v227, 0x22800, v218
	v_add_u32_e32 v228, 0x23000, v218
	s_or_b64 s[62:63], vcc, s[62:63]
	s_waitcnt vmcnt(8)
	v_pk_add_f32 v[6:7], v[12:13], 1.0 op_sel_hi:[1,0]
	s_nop 0
	v_pk_mul_f32 v[6:7], v[10:11], v[6:7]
	s_waitcnt vmcnt(7)
	ds_write_b32 v15, v5
	ds_write_b32 v9, v6
	ds_write_b32 v14, v7
	s_waitcnt vmcnt(6)
	ds_write_b32 v16, v8
	s_waitcnt vmcnt(2)
	v_pk_add_f32 v[218:219], v[224:225], 1.0 op_sel_hi:[1,0]
	s_nop 0
	v_pk_mul_f32 v[218:219], v[222:223], v[218:219]
	s_waitcnt vmcnt(1)
	ds_write_b32 v227, v216
	ds_write_b32 v221, v218
	ds_write_b32 v226, v219
	s_waitcnt vmcnt(0)
	ds_write_b32 v228, v220
